# speedup vs baseline: 1.0088x; 1.0088x over previous
.Lpp_z2:
	v_xor_b32_e32 v59, 16, v58
	v_lshlrev_b32_e32 v59, 2, v59
	v_xor_b32_e32 v61, 32, v58
	v_lshlrev_b32_e32 v61, 2, v61
	s_mul_i32 s3, s15, 0x900
	v_mul_u32_u24_e32 v57, 0x90, v62
	v_lshl_add_u32 v57, v63, 4, v57
	v_add_u32_e32 v57, s3, v57
	v_mul_u32_u24_e32 v56, 0x480, v62
	v_mul_u32_u24_e32 v55, 0x90, v63
	v_add3_u32 v56, v56, v55, s3
	s_lshl_b32 s6, s15, 1
	v_lshrrev_b32_e32 v55, 2, v63
	v_and_b32_e32 v54, 1, v63
	v_mul_u32_u24_e32 v55, 0xc00, v55
	v_lshl_or_b32 v55, v54, 9, v55
	v_add_u32_e32 v54, s6, v62
	v_lshl_or_b32 v55, v54, 4, v55
	v_mov_b32_e32 v52, 1.0
	s_mul_i32 s6, s8, 0x1800
	s_add_u32 s10, s22, s6
	s_addc_u32 s11, s23, 0
	s_waitcnt vmcnt(1)
	v_pk_mul_f32 v[10:11], v[2:3], v[2:3]
	v_pk_fma_f32 v[10:11], v[4:5], v[4:5], v[10:11]
	s_waitcnt vmcnt(0)
	v_pk_mul_f32 v[12:13], v[6:7], v[6:7]
	v_pk_fma_f32 v[12:13], v[8:9], v[8:9], v[12:13]
	v_add_f32_e32 v10, v10, v11
	v_add_f32_e32 v12, v12, v13
	s_nop 1
	v_add_f32_dpp v10, v10, v10 quad_perm:[1,0,3,2] row_mask:0xf bank_mask:0xf bound_ctrl:1
	v_add_f32_dpp v12, v12, v12 quad_perm:[1,0,3,2] row_mask:0xf bank_mask:0xf bound_ctrl:1
	s_nop 1
	v_add_f32_dpp v10, v10, v10 quad_perm:[2,3,0,1] row_mask:0xf bank_mask:0xf bound_ctrl:1
	v_add_f32_dpp v12, v12, v12 quad_perm:[2,3,0,1] row_mask:0xf bank_mask:0xf bound_ctrl:1
	s_nop 1
	v_add_f32_dpp v10, v10, v10 row_half_mirror row_mask:0xf bank_mask:0xf bound_ctrl:1
	v_add_f32_dpp v12, v12, v12 row_half_mirror row_mask:0xf bank_mask:0xf bound_ctrl:1
	s_nop 1
	v_add_f32_dpp v10, v10, v10 row_mirror row_mask:0xf bank_mask:0xf bound_ctrl:1
	v_add_f32_dpp v12, v12, v12 row_mirror row_mask:0xf bank_mask:0xf bound_ctrl:1
	ds_bpermute_b32 v11, v59, v10
	ds_bpermute_b32 v13, v59, v12
	s_waitcnt lgkmcnt(1)
	v_add_f32_e32 v10, v10, v11
	s_waitcnt lgkmcnt(0)
	v_add_f32_e32 v12, v12, v13
	ds_bpermute_b32 v11, v61, v10
	ds_bpermute_b32 v13, v61, v12
	s_waitcnt lgkmcnt(1)
	v_add_f32_e32 v10, v10, v11
	s_waitcnt lgkmcnt(0)
	v_add_f32_e32 v12, v12, v13
	v_rsq_f32_e32 v10, v10
	v_rsq_f32_e32 v12, v12
	s_nop 0
	v_min_f32_e32 v10, 0x4cbebc20, v10
	v_min_f32_e32 v12, 0x4cbebc20, v12
	v_mul_f32_e32 v10, s14, v10
	v_mul_f32_e32 v12, s14, v12
	v_pk_mul_f32 v[2:3], v[2:3], v[10:11] op_sel_hi:[1,0]
	v_pk_mul_f32 v[4:5], v[4:5], v[10:11] op_sel_hi:[1,0]
	v_pk_mul_f32 v[6:7], v[6:7], v[12:13] op_sel_hi:[1,0]
	v_pk_mul_f32 v[8:9], v[8:9], v[12:13] op_sel_hi:[1,0]
	ds_write_b128 v57, v[2:5]
	ds_write_b128 v57, v[6:9] offset:1152
	s_nop 1
	v_pk_add_f32 v[2:3], v[2:3], v[6:7]
	v_pk_add_f32 v[4:5], v[4:5], v[8:9]
	s_mov_b64 exec, 0xffff
	ds_read_b128 v[12:15], v56
	ds_read_b128 v[16:19], v56 offset:16
	ds_read_b128 v[20:23], v56 offset:32
	ds_read_b128 v[24:27], v56 offset:48
	ds_read_b128 v[28:31], v56 offset:64
	ds_read_b128 v[32:35], v56 offset:80
	ds_read_b128 v[36:39], v56 offset:96
	ds_read_b128 v[40:43], v56 offset:112
	v_mov_b32_e32 v50, 0
	v_mov_b32_e32 v51, 0
	s_waitcnt lgkmcnt(0)
	v_cvt_scalef32_2xpk16_fp6_f32 v[44:49], v[12:27], v[28:43], v52
	s_nop 1
	v_mov_b32_e32 v50, v44
	v_mov_b32_e32 v51, v45
	s_nop 1
	v_mov_b32_dpp v50, v44 row_shl:2 row_mask:0xf bank_mask:0xf
	v_mov_b32_dpp v51, v45 row_shl:2 row_mask:0xf bank_mask:0xf
	s_mov_b64 exec, 0x3333
	global_store_dwordx4 v55, v[44:47], s[10:11]
	global_store_dwordx4 v55, v[48:51], s[10:11] offset:1024
	s_mov_b64 exec, 0xcccc
	global_store_dwordx4 v55, v[46:49], s[10:11] offset:2048
	s_mov_b64 exec, -1
	s_cmp_lt_u32 s8, 0x100
	s_cbranch_scc0 .Lpp_end
	v_add_u32_e32 v10, s3, v60
	ds_write_b128 v10, v[2:5]
	s_waitcnt lgkmcnt(0)
	s_barrier
	s_sub_u32 s6, s15, 8
	s_cmp_gt_u32 s6, 3
	s_cbranch_scc1 .Lpp_end
	s_lshl_b32 s6, s6, 8
	v_lshl_add_u32 v10, v58, 2, s6
	ds_read_b32 v12, v10
	ds_read_b32 v13, v10 offset:2304
	ds_read_b32 v14, v10 offset:4608
	ds_read_b32 v15, v10 offset:6912
	ds_read_b32 v16, v10 offset:9216
	ds_read_b32 v17, v10 offset:11520
	ds_read_b32 v18, v10 offset:13824
	ds_read_b32 v19, v10 offset:16128
	ds_read_b32 v20, v10 offset:18432
	ds_read_b32 v21, v10 offset:20736
	ds_read_b32 v22, v10 offset:23040
	ds_read_b32 v23, v10 offset:25344
	ds_read_b32 v24, v10 offset:27648
	ds_read_b32 v25, v10 offset:29952
	ds_read_b32 v26, v10 offset:32256
	ds_read_b32 v27, v10 offset:34560
	s_cmp_lt_u32 s8, 0x80
	s_cselect_b32 s10, s24, s26
	s_cselect_b32 s11, s25, s27
	s_and_b32 s6, s8, 0x7f
	s_lshl_b32 s6, s6, 10
	s_add_u32 s10, s10, s6
	s_addc_u32 s11, s11, 0
	s_waitcnt lgkmcnt(14)
	v_add_f32_e32 v12, v12, v13
	s_waitcnt lgkmcnt(13)
	v_add_f32_e32 v12, v12, v14
	s_waitcnt lgkmcnt(12)
	v_add_f32_e32 v12, v12, v15
	s_waitcnt lgkmcnt(11)
	v_add_f32_e32 v12, v12, v16
	s_waitcnt lgkmcnt(10)
	v_add_f32_e32 v12, v12, v17
	s_waitcnt lgkmcnt(9)
	v_add_f32_e32 v12, v12, v18
	s_waitcnt lgkmcnt(8)
	v_add_f32_e32 v12, v12, v19
	s_waitcnt lgkmcnt(7)
	v_add_f32_e32 v12, v12, v20
	s_waitcnt lgkmcnt(6)
	v_add_f32_e32 v12, v12, v21
	s_waitcnt lgkmcnt(5)
	v_add_f32_e32 v12, v12, v22
	s_waitcnt lgkmcnt(4)
	v_add_f32_e32 v12, v12, v23
	s_waitcnt lgkmcnt(3)
	v_add_f32_e32 v12, v12, v24
	s_waitcnt lgkmcnt(2)
	v_add_f32_e32 v12, v12, v25
	s_waitcnt lgkmcnt(1)
	v_add_f32_e32 v12, v12, v26
	s_waitcnt lgkmcnt(0)
	v_add_f32_e32 v12, v12, v27
	global_store_dword v10, v12, s[10:11]

.Lmk_start:
	s_mov_b32 s28, s8
	s_mov_b64 s[30:31], s[4:5]
	s_mov_b64 s[32:33], s[6:7]
	s_mov_b64 s[6:7], s[2:3]
	s_mov_b64 s[34:35], s[2:3]
	s_mov_b32 s2, s28
	s_and_b32 s3, s2, 7
	s_lshr_b32 s4, s2, 3
	s_and_b32 s5, s4, 3
	s_lshl_b32 s3, s3, 2
	s_or_b32 s8, s3, s5
	s_lshr_b32 s9, s4, 2
	v_lshrrev_b32_e32 v127, 6, v0
	v_and_b32_e32 v124, 63, v0
	v_lshlrev_b32_e32 v125, 3, v124
	v_lshlrev_b32_e32 v124, 4, v124
	v_readfirstlane_b32 s12, v127
	v_mov_b32_e32 v120, 0
	v_mov_b32_e32 v121, 0
	v_mov_b32_e32 v122, 0
	v_mov_b32_e32 v123, 0
	s_lshl_b32 s13, s12, 10
	s_lshl_b32 s14, s9, 3
	s_add_u32 s14, s14, s12
	s_mul_i32 s15, s14, 0x1800
	s_mul_i32 s16, s8, 0x12000
	s_add_u32 s16, s16, 0xc0000
	s_add_u32 s16, s16, s13
	s_add_u32 s20, s13, 0x2000
	s_add_u32 s10, s6, s16
	s_addc_u32 s11, s7, 0
	s_add_u32 s18, s6, s15
	s_addc_u32 s19, s7, 0
	s_add_u32 s22, s18, 0xc00
	s_addc_u32 s23, s19, 0
	s_cmp_lt_u32 s12, 4
	s_cbranch_scc0 .Lmk_vb
	s_mov_b32 m0, s13
	s_nop 0
	global_load_lds_dwordx4 v124, s[10:11]
	s_add_u32 s26, s10, 0x2000
	s_addc_u32 s27, s11, 0
	s_mov_b32 m0, s20
	s_nop 0
	global_load_lds_dwordx4 v124, s[26:27]
	global_load_dwordx4 v[96:99], v124, s[18:19]
	global_load_dwordx4 v[100:103], v124, s[18:19] offset:1024
	global_load_dwordx4 v[104:107], v124, s[18:19] offset:2048
	global_load_dwordx4 v[108:111], v124, s[22:23]
	global_load_dwordx4 v[112:115], v124, s[22:23] offset:1024
	global_load_dwordx4 v[116:119], v124, s[22:23] offset:2048
	s_add_u32 s24, s10, 0x3000
	s_addc_u32 s25, s11, 0
	s_add_u32 s26, s13, 0x3000
	s_mov_b32 m0, s26
	s_nop 0
	global_load_lds_dwordx4 v124, s[24:25]
	s_add_u32 s26, s24, 0x2000
	s_addc_u32 s27, s25, 0
	s_add_u32 s29, s20, 0x3000
	s_mov_b32 m0, s29
	s_nop 0
	global_load_lds_dwordx4 v124, s[26:27]
	s_add_u32 s24, s10, 0x6000
	s_addc_u32 s25, s11, 0
	s_add_u32 s26, s13, 0x6000
	s_mov_b32 m0, s26
	s_nop 0
	global_load_lds_dwordx4 v124, s[24:25]
	s_add_u32 s26, s24, 0x2000
	s_addc_u32 s27, s25, 0
	s_add_u32 s29, s20, 0x6000
	s_mov_b32 m0, s29
	s_nop 0
	global_load_lds_dwordx4 v124, s[26:27]
	s_add_u32 s24, s10, 0x9000
	s_addc_u32 s25, s11, 0
	s_add_u32 s26, s13, 0x9000
	s_mov_b32 m0, s26
	s_nop 0
	global_load_lds_dwordx4 v124, s[24:25]
	s_add_u32 s26, s24, 0x2000
	s_addc_u32 s27, s25, 0
	s_add_u32 s29, s20, 0x9000
	s_mov_b32 m0, s29
	s_nop 0
	global_load_lds_dwordx4 v124, s[26:27]
	s_add_u32 s24, s10, 0xc000
	s_addc_u32 s25, s11, 0
	s_add_u32 s26, s13, 0xc000
	s_mov_b32 m0, s26
	s_nop 0
	global_load_lds_dwordx4 v124, s[24:25]
	s_add_u32 s26, s24, 0x2000
	s_addc_u32 s27, s25, 0
	s_add_u32 s29, s20, 0xc000
	s_mov_b32 m0, s29
	s_nop 0
	global_load_lds_dwordx4 v124, s[26:27]
	s_waitcnt vmcnt(8)
	s_barrier
	ds_read_b128 v[0:3], v124
	ds_read_b128 v[4:7], v124 offset:1024
	ds_read_b128 v[8:11], v124 offset:2048
	ds_read_b128 v[12:15], v124 offset:3072
	ds_read_b128 v[16:19], v124 offset:4096
	ds_read_b128 v[20:23], v124 offset:5120
	s_waitcnt lgkmcnt(0)
	s_setprio 2
	v_mfma_f32_32x32x64_f8f6f4 v[48:63], v[0:5], v[96:101], 0 cbsz:2 blgp:2
	ds_read_b128 v[24:27], v124 offset:6144
	v_mfma_f32_32x32x64_f8f6f4 v[48:63], v[6:11], v[102:107], v[48:63] cbsz:2 blgp:2
	ds_read_b128 v[28:31], v124 offset:7168
	ds_read_b128 v[32:35], v124 offset:8192
	v_mfma_f32_32x32x64_f8f6f4 v[48:63], v[12:17], v[108:113], v[48:63] cbsz:2 blgp:2
	ds_read_b128 v[36:39], v124 offset:9216
	v_mfma_f32_32x32x64_f8f6f4 v[48:63], v[18:23], v[114:119], v[48:63] cbsz:2 blgp:2
	ds_read_b128 v[40:43], v124 offset:10240
	ds_read_b128 v[44:47], v124 offset:11264
	s_waitcnt vmcnt(6) lgkmcnt(0)
	s_barrier
	s_add_u32 s24, s10, 0xf000
	s_addc_u32 s25, s11, 0
	s_mov_b32 m0, s13
	s_nop 0
	global_load_lds_dwordx4 v124, s[24:25]
	s_add_u32 s26, s24, 0x2000
	s_addc_u32 s27, s25, 0
	s_mov_b32 m0, s20
	s_nop 0
	global_load_lds_dwordx4 v124, s[26:27]
	v_mfma_f32_32x32x64_f8f6f4 v[64:79], v[24:29], v[96:101], 0 cbsz:2 blgp:2
	ds_read_b128 v[0:3], v124 offset:12288
	ds_read_b128 v[4:7], v124 offset:13312
	ds_read_b128 v[8:11], v124 offset:14336
	ds_read_b128 v[24:27], v124 offset:18432
	v_mfma_f32_32x32x64_f8f6f4 v[64:79], v[30:35], v[102:107], v[64:79] cbsz:2 blgp:2
	ds_read_b128 v[12:15], v124 offset:15360
	ds_read_b128 v[16:19], v124 offset:16384
	ds_read_b128 v[20:23], v124 offset:17408
	ds_read_b128 v[28:31], v124 offset:19456
	ds_read_b128 v[32:35], v124 offset:20480
	v_exp_f32_e32 v48, v48
	v_exp_f32_e32 v49, v49
	v_exp_f32_e32 v50, v50
	v_exp_f32_e32 v51, v51
	v_mfma_f32_32x32x64_f8f6f4 v[64:79], v[36:41], v[108:113], v[64:79] cbsz:2 blgp:2
	ds_read_b128 v[36:39], v124 offset:21504
	v_exp_f32_e32 v52, v52
	v_exp_f32_e32 v53, v53
	v_exp_f32_e32 v54, v54
	v_exp_f32_e32 v55, v55
	v_pk_add_f32 v[120:121], v[120:121], v[48:49]
	v_pk_add_f32 v[122:123], v[122:123], v[50:51]
	v_mfma_f32_32x32x64_f8f6f4 v[64:79], v[42:47], v[114:119], v[64:79] cbsz:2 blgp:2
	ds_read_b128 v[40:43], v124 offset:22528
	ds_read_b128 v[44:47], v124 offset:23552
	v_exp_f32_e32 v56, v56
	v_exp_f32_e32 v57, v57
	v_exp_f32_e32 v58, v58
	v_exp_f32_e32 v59, v59
	v_pk_add_f32 v[120:121], v[120:121], v[52:53]
	v_pk_add_f32 v[122:123], v[122:123], v[54:55]
	s_waitcnt vmcnt(6) lgkmcnt(5)
	s_barrier
	v_mfma_f32_32x32x64_f8f6f4 v[80:95], v[0:5], v[96:101], 0 cbsz:2 blgp:2
	ds_read_b128 v[0:3], v124 offset:24576
	v_exp_f32_e32 v60, v60
	v_exp_f32_e32 v61, v61
	v_exp_f32_e32 v62, v62
	v_exp_f32_e32 v63, v63
	v_pk_add_f32 v[120:121], v[120:121], v[56:57]
	v_pk_add_f32 v[122:123], v[122:123], v[58:59]
	v_mfma_f32_32x32x64_f8f6f4 v[80:95], v[6:11], v[102:107], v[80:95] cbsz:2 blgp:2
	ds_read_b128 v[4:7], v124 offset:25600
	ds_read_b128 v[8:11], v124 offset:26624
	v_exp_f32_e32 v64, v64
	v_exp_f32_e32 v65, v65
	v_exp_f32_e32 v66, v66
	v_exp_f32_e32 v67, v67
	v_pk_add_f32 v[120:121], v[120:121], v[60:61]
	v_pk_add_f32 v[122:123], v[122:123], v[62:63]
	v_mfma_f32_32x32x64_f8f6f4 v[80:95], v[12:17], v[108:113], v[80:95] cbsz:2 blgp:2
	ds_read_b128 v[12:15], v124 offset:27648
	v_exp_f32_e32 v68, v68
	v_exp_f32_e32 v69, v69
	v_exp_f32_e32 v70, v70
	v_exp_f32_e32 v71, v71
	v_pk_add_f32 v[120:121], v[120:121], v[64:65]
	v_pk_add_f32 v[122:123], v[122:123], v[66:67]
	v_mfma_f32_32x32x64_f8f6f4 v[80:95], v[18:23], v[114:119], v[80:95] cbsz:2 blgp:2
	ds_read_b128 v[16:19], v124 offset:28672
	ds_read_b128 v[20:23], v124 offset:29696
	v_exp_f32_e32 v72, v72
	v_exp_f32_e32 v73, v73
	v_exp_f32_e32 v74, v74
	v_exp_f32_e32 v75, v75
	v_pk_add_f32 v[120:121], v[120:121], v[68:69]
	v_pk_add_f32 v[122:123], v[122:123], v[70:71]
	s_waitcnt lgkmcnt(6)
	v_mfma_f32_32x32x64_f8f6f4 v[48:63], v[24:29], v[96:101], 0 cbsz:2 blgp:2
	ds_read_b128 v[24:27], v124 offset:30720
	v_exp_f32_e32 v76, v76
	v_exp_f32_e32 v77, v77
	v_exp_f32_e32 v78, v78
	v_exp_f32_e32 v79, v79
	v_pk_add_f32 v[120:121], v[120:121], v[72:73]
	v_pk_add_f32 v[122:123], v[122:123], v[74:75]
	v_mfma_f32_32x32x64_f8f6f4 v[48:63], v[30:35], v[102:107], v[48:63] cbsz:2 blgp:2
	ds_read_b128 v[28:31], v124 offset:31744
	ds_read_b128 v[32:35], v124 offset:32768
	v_exp_f32_e32 v80, v80
	v_exp_f32_e32 v81, v81
	v_exp_f32_e32 v82, v82
	v_exp_f32_e32 v83, v83
	v_pk_add_f32 v[120:121], v[120:121], v[76:77]
	v_pk_add_f32 v[122:123], v[122:123], v[78:79]
	v_mfma_f32_32x32x64_f8f6f4 v[48:63], v[36:41], v[108:113], v[48:63] cbsz:2 blgp:2
	ds_read_b128 v[36:39], v124 offset:33792
	v_exp_f32_e32 v84, v84
	v_exp_f32_e32 v85, v85
	v_exp_f32_e32 v86, v86
	v_exp_f32_e32 v87, v87
	v_pk_add_f32 v[120:121], v[120:121], v[80:81]
	v_pk_add_f32 v[122:123], v[122:123], v[82:83]
	v_mfma_f32_32x32x64_f8f6f4 v[48:63], v[42:47], v[114:119], v[48:63] cbsz:2 blgp:2
	ds_read_b128 v[40:43], v124 offset:34816
	ds_read_b128 v[44:47], v124 offset:35840
	v_exp_f32_e32 v88, v88
	v_exp_f32_e32 v89, v89
	v_exp_f32_e32 v90, v90
	v_exp_f32_e32 v91, v91
	v_pk_add_f32 v[120:121], v[120:121], v[84:85]
	v_pk_add_f32 v[122:123], v[122:123], v[86:87]
	s_setprio 1
	s_waitcnt vmcnt(4) lgkmcnt(6)
	s_barrier
	v_mfma_f32_32x32x64_f8f6f4 v[64:79], v[0:5], v[96:101], 0 cbsz:2 blgp:2
	ds_read_b128 v[0:3], v124 offset:36864
	v_exp_f32_e32 v92, v92
	v_exp_f32_e32 v93, v93
	v_exp_f32_e32 v94, v94
	v_exp_f32_e32 v95, v95
	v_pk_add_f32 v[120:121], v[120:121], v[88:89]
	v_pk_add_f32 v[122:123], v[122:123], v[90:91]
	v_mfma_f32_32x32x64_f8f6f4 v[64:79], v[6:11], v[102:107], v[64:79] cbsz:2 blgp:2
	ds_read_b128 v[4:7], v124 offset:37888
	ds_read_b128 v[8:11], v124 offset:38912
	v_exp_f32_e32 v48, v48
	v_exp_f32_e32 v49, v49
	v_exp_f32_e32 v50, v50
	v_exp_f32_e32 v51, v51
	v_pk_add_f32 v[120:121], v[120:121], v[92:93]
	v_pk_add_f32 v[122:123], v[122:123], v[94:95]
	v_mfma_f32_32x32x64_f8f6f4 v[64:79], v[12:17], v[108:113], v[64:79] cbsz:2 blgp:2
	ds_read_b128 v[12:15], v124 offset:39936
	v_exp_f32_e32 v52, v52
	v_exp_f32_e32 v53, v53
	v_exp_f32_e32 v54, v54
	v_exp_f32_e32 v55, v55
	v_pk_add_f32 v[120:121], v[120:121], v[48:49]
	v_pk_add_f32 v[122:123], v[122:123], v[50:51]
	v_mfma_f32_32x32x64_f8f6f4 v[64:79], v[18:23], v[114:119], v[64:79] cbsz:2 blgp:2
	ds_read_b128 v[16:19], v124 offset:40960
	ds_read_b128 v[20:23], v124 offset:41984
	v_exp_f32_e32 v56, v56
	v_exp_f32_e32 v57, v57
	v_exp_f32_e32 v58, v58
	v_exp_f32_e32 v59, v59
	v_pk_add_f32 v[120:121], v[120:121], v[52:53]
	v_pk_add_f32 v[122:123], v[122:123], v[54:55]
	s_waitcnt lgkmcnt(6)
	v_mfma_f32_32x32x64_f8f6f4 v[80:95], v[24:29], v[96:101], 0 cbsz:2 blgp:2
	ds_read_b128 v[24:27], v124 offset:43008
	v_exp_f32_e32 v60, v60
	v_exp_f32_e32 v61, v61
	v_exp_f32_e32 v62, v62
	v_exp_f32_e32 v63, v63
	v_pk_add_f32 v[120:121], v[120:121], v[56:57]
	v_pk_add_f32 v[122:123], v[122:123], v[58:59]
	v_mfma_f32_32x32x64_f8f6f4 v[80:95], v[30:35], v[102:107], v[80:95] cbsz:2 blgp:2
	ds_read_b128 v[28:31], v124 offset:44032
	ds_read_b128 v[32:35], v124 offset:45056
	v_exp_f32_e32 v64, v64
	v_exp_f32_e32 v65, v65
	v_exp_f32_e32 v66, v66
	v_exp_f32_e32 v67, v67
	v_pk_add_f32 v[120:121], v[120:121], v[60:61]
	v_pk_add_f32 v[122:123], v[122:123], v[62:63]
	v_mfma_f32_32x32x64_f8f6f4 v[80:95], v[36:41], v[108:113], v[80:95] cbsz:2 blgp:2
	ds_read_b128 v[36:39], v124 offset:46080
	v_exp_f32_e32 v68, v68
	v_exp_f32_e32 v69, v69
	v_exp_f32_e32 v70, v70
	v_exp_f32_e32 v71, v71
	v_pk_add_f32 v[120:121], v[120:121], v[64:65]
	v_pk_add_f32 v[122:123], v[122:123], v[66:67]
	v_mfma_f32_32x32x64_f8f6f4 v[80:95], v[42:47], v[114:119], v[80:95] cbsz:2 blgp:2
	ds_read_b128 v[40:43], v124 offset:47104
	ds_read_b128 v[44:47], v124 offset:48128
	v_exp_f32_e32 v72, v72
	v_exp_f32_e32 v73, v73
	v_exp_f32_e32 v74, v74
	v_exp_f32_e32 v75, v75
	v_pk_add_f32 v[120:121], v[120:121], v[68:69]
	v_pk_add_f32 v[122:123], v[122:123], v[70:71]
	s_waitcnt vmcnt(2) lgkmcnt(6)
	s_barrier
	v_mfma_f32_32x32x64_f8f6f4 v[48:63], v[0:5], v[96:101], 0 cbsz:2 blgp:2
	ds_read_b128 v[0:3], v124 offset:49152
	v_exp_f32_e32 v76, v76
	v_exp_f32_e32 v77, v77
	v_exp_f32_e32 v78, v78
	v_exp_f32_e32 v79, v79
	v_pk_add_f32 v[120:121], v[120:121], v[72:73]
	v_pk_add_f32 v[122:123], v[122:123], v[74:75]
	v_mfma_f32_32x32x64_f8f6f4 v[48:63], v[6:11], v[102:107], v[48:63] cbsz:2 blgp:2
	ds_read_b128 v[4:7], v124 offset:50176
	ds_read_b128 v[8:11], v124 offset:51200
	v_exp_f32_e32 v80, v80
	v_exp_f32_e32 v81, v81
	v_exp_f32_e32 v82, v82
	v_exp_f32_e32 v83, v83
	v_pk_add_f32 v[120:121], v[120:121], v[76:77]
	v_pk_add_f32 v[122:123], v[122:123], v[78:79]
	v_mfma_f32_32x32x64_f8f6f4 v[48:63], v[12:17], v[108:113], v[48:63] cbsz:2 blgp:2
	ds_read_b128 v[12:15], v124 offset:52224
	v_exp_f32_e32 v84, v84
	v_exp_f32_e32 v85, v85
	v_exp_f32_e32 v86, v86
	v_exp_f32_e32 v87, v87
	v_pk_add_f32 v[120:121], v[120:121], v[80:81]
	v_pk_add_f32 v[122:123], v[122:123], v[82:83]
	v_mfma_f32_32x32x64_f8f6f4 v[48:63], v[18:23], v[114:119], v[48:63] cbsz:2 blgp:2
	ds_read_b128 v[16:19], v124 offset:53248
	ds_read_b128 v[20:23], v124 offset:54272
	v_exp_f32_e32 v88, v88
	v_exp_f32_e32 v89, v89
	v_exp_f32_e32 v90, v90
	v_exp_f32_e32 v91, v91
	v_pk_add_f32 v[120:121], v[120:121], v[84:85]
	v_pk_add_f32 v[122:123], v[122:123], v[86:87]
	s_waitcnt lgkmcnt(6)
	v_mfma_f32_32x32x64_f8f6f4 v[64:79], v[24:29], v[96:101], 0 cbsz:2 blgp:2
	ds_read_b128 v[24:27], v124 offset:55296
	v_exp_f32_e32 v92, v92
	v_exp_f32_e32 v93, v93
	v_exp_f32_e32 v94, v94
	v_exp_f32_e32 v95, v95
	v_pk_add_f32 v[120:121], v[120:121], v[88:89]
	v_pk_add_f32 v[122:123], v[122:123], v[90:91]
	v_mfma_f32_32x32x64_f8f6f4 v[64:79], v[30:35], v[102:107], v[64:79] cbsz:2 blgp:2
	ds_read_b128 v[28:31], v124 offset:56320
	ds_read_b128 v[32:35], v124 offset:57344
	v_exp_f32_e32 v48, v48
	v_exp_f32_e32 v49, v49
	v_exp_f32_e32 v50, v50
	v_exp_f32_e32 v51, v51
	v_pk_add_f32 v[120:121], v[120:121], v[92:93]
	v_pk_add_f32 v[122:123], v[122:123], v[94:95]
	v_mfma_f32_32x32x64_f8f6f4 v[64:79], v[36:41], v[108:113], v[64:79] cbsz:2 blgp:2
	ds_read_b128 v[36:39], v124 offset:58368
	v_exp_f32_e32 v52, v52
	v_exp_f32_e32 v53, v53
	v_exp_f32_e32 v54, v54
	v_exp_f32_e32 v55, v55
	v_pk_add_f32 v[120:121], v[120:121], v[48:49]
	v_pk_add_f32 v[122:123], v[122:123], v[50:51]
	v_mfma_f32_32x32x64_f8f6f4 v[64:79], v[42:47], v[114:119], v[64:79] cbsz:2 blgp:2
	ds_read_b128 v[40:43], v124 offset:59392
	ds_read_b128 v[44:47], v124 offset:60416
	v_exp_f32_e32 v56, v56
	v_exp_f32_e32 v57, v57
	v_exp_f32_e32 v58, v58
	v_exp_f32_e32 v59, v59
	v_pk_add_f32 v[120:121], v[120:121], v[52:53]
	v_pk_add_f32 v[122:123], v[122:123], v[54:55]
	s_setprio 0
	s_waitcnt vmcnt(0) lgkmcnt(6)
	s_barrier
	v_mfma_f32_32x32x64_f8f6f4 v[80:95], v[0:5], v[96:101], 0 cbsz:2 blgp:2
	ds_read_b128 v[0:3], v124
	v_exp_f32_e32 v60, v60
	v_exp_f32_e32 v61, v61
	v_exp_f32_e32 v62, v62
	v_exp_f32_e32 v63, v63
	v_pk_add_f32 v[120:121], v[120:121], v[56:57]
	v_pk_add_f32 v[122:123], v[122:123], v[58:59]
	v_mfma_f32_32x32x64_f8f6f4 v[80:95], v[6:11], v[102:107], v[80:95] cbsz:2 blgp:2
	ds_read_b128 v[4:7], v124 offset:1024
	ds_read_b128 v[8:11], v124 offset:2048
	v_exp_f32_e32 v64, v64
	v_exp_f32_e32 v65, v65
	v_exp_f32_e32 v66, v66
	v_exp_f32_e32 v67, v67
	v_pk_add_f32 v[120:121], v[120:121], v[60:61]
	v_pk_add_f32 v[122:123], v[122:123], v[62:63]
	v_mfma_f32_32x32x64_f8f6f4 v[80:95], v[12:17], v[108:113], v[80:95] cbsz:2 blgp:2
	ds_read_b128 v[12:15], v124 offset:3072
	v_exp_f32_e32 v68, v68
	v_exp_f32_e32 v69, v69
	v_exp_f32_e32 v70, v70
	v_exp_f32_e32 v71, v71
	v_pk_add_f32 v[120:121], v[120:121], v[64:65]
	v_pk_add_f32 v[122:123], v[122:123], v[66:67]
	v_mfma_f32_32x32x64_f8f6f4 v[80:95], v[18:23], v[114:119], v[80:95] cbsz:2 blgp:2
	ds_read_b128 v[16:19], v124 offset:4096
	ds_read_b128 v[20:23], v124 offset:5120
	v_exp_f32_e32 v72, v72
	v_exp_f32_e32 v73, v73
	v_exp_f32_e32 v74, v74
	v_exp_f32_e32 v75, v75
	v_pk_add_f32 v[120:121], v[120:121], v[68:69]
	v_pk_add_f32 v[122:123], v[122:123], v[70:71]
	s_waitcnt lgkmcnt(6)
	v_mfma_f32_32x32x64_f8f6f4 v[48:63], v[24:29], v[96:101], 0 cbsz:2 blgp:2
	ds_read_b128 v[24:27], v124 offset:6144
	v_exp_f32_e32 v76, v76
	v_exp_f32_e32 v77, v77
	v_exp_f32_e32 v78, v78
	v_exp_f32_e32 v79, v79
	v_pk_add_f32 v[120:121], v[120:121], v[72:73]
	v_pk_add_f32 v[122:123], v[122:123], v[74:75]
	v_mfma_f32_32x32x64_f8f6f4 v[48:63], v[30:35], v[102:107], v[48:63] cbsz:2 blgp:2
	ds_read_b128 v[28:31], v124 offset:7168
	ds_read_b128 v[32:35], v124 offset:8192
	v_exp_f32_e32 v80, v80
	v_exp_f32_e32 v81, v81
	v_exp_f32_e32 v82, v82
	v_exp_f32_e32 v83, v83
	v_pk_add_f32 v[120:121], v[120:121], v[76:77]
	v_pk_add_f32 v[122:123], v[122:123], v[78:79]
	s_cmp_lg_u32 s8, 10
	s_cbranch_scc1 .Lmk_nosplit_a
	v_add_f32_e32 v127, v120, v121
	v_add_f32_e32 v126, v122, v123
	v_mov_b32_e32 v120, 0
	v_mov_b32_e32 v121, 0
	v_mov_b32_e32 v122, 0
	v_mov_b32_e32 v123, 0
	v_add_f32_e32 v127, v127, v126
.Lmk_nosplit_a:
	v_mfma_f32_32x32x64_f8f6f4 v[48:63], v[36:41], v[108:113], v[48:63] cbsz:2 blgp:2
	ds_read_b128 v[36:39], v124 offset:9216
	v_exp_f32_e32 v84, v84
	v_exp_f32_e32 v85, v85
	v_exp_f32_e32 v86, v86
	v_exp_f32_e32 v87, v87
	v_pk_add_f32 v[120:121], v[120:121], v[80:81]
	v_pk_add_f32 v[122:123], v[122:123], v[82:83]
	v_mfma_f32_32x32x64_f8f6f4 v[48:63], v[42:47], v[114:119], v[48:63] cbsz:2 blgp:2
	ds_read_b128 v[40:43], v124 offset:10240
	ds_read_b128 v[44:47], v124 offset:11264
	v_exp_f32_e32 v88, v88
	v_exp_f32_e32 v89, v89
	v_exp_f32_e32 v90, v90
	v_exp_f32_e32 v91, v91
	v_pk_add_f32 v[120:121], v[120:121], v[84:85]
	v_pk_add_f32 v[122:123], v[122:123], v[86:87]
	s_waitcnt lgkmcnt(6)
	v_mfma_f32_32x32x64_f8f6f4 v[64:79], v[0:5], v[96:101], 0 cbsz:2 blgp:2
	v_exp_f32_e32 v92, v92
	v_exp_f32_e32 v93, v93
	v_exp_f32_e32 v94, v94
	v_exp_f32_e32 v95, v95
	v_pk_add_f32 v[120:121], v[120:121], v[88:89]
	v_pk_add_f32 v[122:123], v[122:123], v[90:91]
	v_mfma_f32_32x32x64_f8f6f4 v[64:79], v[6:11], v[102:107], v[64:79] cbsz:2 blgp:2
	v_exp_f32_e32 v48, v48
	v_exp_f32_e32 v49, v49
	v_exp_f32_e32 v50, v50
	v_exp_f32_e32 v51, v51
	v_pk_add_f32 v[120:121], v[120:121], v[92:93]
	v_pk_add_f32 v[122:123], v[122:123], v[94:95]
	v_mfma_f32_32x32x64_f8f6f4 v[64:79], v[12:17], v[108:113], v[64:79] cbsz:2 blgp:2
	v_exp_f32_e32 v52, v52
	v_exp_f32_e32 v53, v53
	v_exp_f32_e32 v54, v54
	v_exp_f32_e32 v55, v55
	v_pk_add_f32 v[120:121], v[120:121], v[48:49]
	v_pk_add_f32 v[122:123], v[122:123], v[50:51]
	v_mfma_f32_32x32x64_f8f6f4 v[64:79], v[18:23], v[114:119], v[64:79] cbsz:2 blgp:2
	v_exp_f32_e32 v56, v56
	v_exp_f32_e32 v57, v57
	v_exp_f32_e32 v58, v58
	v_exp_f32_e32 v59, v59
	v_pk_add_f32 v[120:121], v[120:121], v[52:53]
	v_pk_add_f32 v[122:123], v[122:123], v[54:55]
	s_waitcnt lgkmcnt(0)
	v_mfma_f32_32x32x64_f8f6f4 v[80:95], v[24:29], v[96:101], 0 cbsz:2 blgp:2
	v_exp_f32_e32 v60, v60
	v_exp_f32_e32 v61, v61
	v_exp_f32_e32 v62, v62
	v_exp_f32_e32 v63, v63
	v_pk_add_f32 v[120:121], v[120:121], v[56:57]
	v_pk_add_f32 v[122:123], v[122:123], v[58:59]
	v_mfma_f32_32x32x64_f8f6f4 v[80:95], v[30:35], v[102:107], v[80:95] cbsz:2 blgp:2
	v_exp_f32_e32 v64, v64
	v_exp_f32_e32 v65, v65
	v_exp_f32_e32 v66, v66
	v_exp_f32_e32 v67, v67
	v_pk_add_f32 v[120:121], v[120:121], v[60:61]
	v_pk_add_f32 v[122:123], v[122:123], v[62:63]
	v_mfma_f32_32x32x64_f8f6f4 v[80:95], v[36:41], v[108:113], v[80:95] cbsz:2 blgp:2
	v_exp_f32_e32 v68, v68
	v_exp_f32_e32 v69, v69
	v_exp_f32_e32 v70, v70
	v_exp_f32_e32 v71, v71
	v_pk_add_f32 v[120:121], v[120:121], v[64:65]
	v_pk_add_f32 v[122:123], v[122:123], v[66:67]
	v_mfma_f32_32x32x64_f8f6f4 v[80:95], v[42:47], v[114:119], v[80:95] cbsz:2 blgp:2
	v_exp_f32_e32 v72, v72
	v_exp_f32_e32 v73, v73
	v_exp_f32_e32 v74, v74
	v_exp_f32_e32 v75, v75
	v_pk_add_f32 v[120:121], v[120:121], v[68:69]
	v_pk_add_f32 v[122:123], v[122:123], v[70:71]
	v_exp_f32_e32 v76, v76
	v_exp_f32_e32 v77, v77
	v_exp_f32_e32 v78, v78
	v_exp_f32_e32 v79, v79
	v_pk_add_f32 v[120:121], v[120:121], v[72:73]
	v_pk_add_f32 v[122:123], v[122:123], v[74:75]
	s_nop 1
	v_exp_f32_e32 v80, v80
	v_exp_f32_e32 v81, v81
	v_exp_f32_e32 v82, v82
	v_exp_f32_e32 v83, v83
	v_pk_add_f32 v[120:121], v[120:121], v[76:77]
	v_pk_add_f32 v[122:123], v[122:123], v[78:79]
	v_exp_f32_e32 v84, v84
	v_exp_f32_e32 v85, v85
	v_exp_f32_e32 v86, v86
	v_exp_f32_e32 v87, v87
	v_pk_add_f32 v[120:121], v[120:121], v[80:81]
	v_pk_add_f32 v[122:123], v[122:123], v[82:83]
	v_exp_f32_e32 v88, v88
	v_exp_f32_e32 v89, v89
	v_exp_f32_e32 v90, v90
	v_exp_f32_e32 v91, v91
	v_pk_add_f32 v[120:121], v[120:121], v[84:85]
	v_pk_add_f32 v[122:123], v[122:123], v[86:87]
	v_exp_f32_e32 v92, v92
	v_exp_f32_e32 v93, v93
	v_exp_f32_e32 v94, v94
	v_exp_f32_e32 v95, v95
	v_pk_add_f32 v[120:121], v[120:121], v[88:89]
	v_pk_add_f32 v[122:123], v[122:123], v[90:91]
	v_pk_add_f32 v[120:121], v[120:121], v[92:93]
	v_pk_add_f32 v[122:123], v[122:123], v[94:95]
	v_add_f32_e32 v120, v120, v121
	v_add_f32_e32 v122, v122, v123
	v_lshrrev_b32_e32 v126, 2, v124
	v_add_f32_e32 v120, v120, v122
	v_xor_b32_e32 v125, 0x80, v126
	s_mov_b64 s[4:5], s[30:31]
	s_mov_b64 s[6:7], s[32:33]
	ds_bpermute_b32 v122, v125, v120
	ds_bpermute_b32 v123, v125, v127
	s_lshl_b32 s14, s14, 7
	v_add_u32_e32 v126, s14, v126
	v_cmp_gt_u32_e32 vcc, 0x200, v124
	s_and_saveexec_b64 s[16:17], vcc
	s_cbranch_execz .Lmk_end_a
	s_waitcnt lgkmcnt(0)
	v_add_f32_e32 v120, v120, v122
	v_add_f32_e32 v127, v127, v123
	s_cmp_lt_u32 s8, 10
	s_cbranch_scc1 .Lmk_pos_only_a
	s_cmp_eq_u32 s8, 10
	s_cbranch_scc0 .Lmk_neg_only_a
	global_atomic_add_f32 v126, v127, s[4:5]

.Lmk_vb:
	s_mov_b32 m0, s13
	s_nop 0
	global_load_lds_dwordx4 v124, s[10:11]
	global_load_dwordx4 v[96:99], v124, s[18:19]
	global_load_dwordx4 v[100:103], v124, s[18:19] offset:1024
	global_load_dwordx4 v[104:107], v124, s[18:19] offset:2048
	global_load_dwordx4 v[108:111], v124, s[22:23]
	global_load_dwordx4 v[112:115], v124, s[22:23] offset:1024
	global_load_dwordx4 v[116:119], v124, s[22:23] offset:2048
	s_add_u32 s24, s10, 0x3000
	s_addc_u32 s25, s11, 0
	s_add_u32 s26, s13, 0x3000
	s_mov_b32 m0, s26
	s_nop 0
	global_load_lds_dwordx4 v124, s[24:25]
	s_add_u32 s24, s10, 0x6000
	s_addc_u32 s25, s11, 0
	s_add_u32 s26, s13, 0x6000
	s_mov_b32 m0, s26
	s_nop 0
	global_load_lds_dwordx4 v124, s[24:25]
	s_add_u32 s24, s10, 0x9000
	s_addc_u32 s25, s11, 0
	s_add_u32 s26, s13, 0x9000
	s_mov_b32 m0, s26
	s_nop 0
	global_load_lds_dwordx4 v124, s[24:25]
	s_add_u32 s24, s10, 0xc000
	s_addc_u32 s25, s11, 0
	s_add_u32 s26, s13, 0xc000
	s_mov_b32 m0, s26
	s_nop 0
	global_load_lds_dwordx4 v124, s[24:25]
	s_waitcnt vmcnt(4)
	s_barrier
	ds_read_b128 v[0:3], v124
	ds_read_b128 v[4:7], v124 offset:1024
	ds_read_b128 v[8:11], v124 offset:2048
	ds_read_b128 v[12:15], v124 offset:3072
	ds_read_b128 v[16:19], v124 offset:4096
	ds_read_b128 v[20:23], v124 offset:5120
	s_waitcnt lgkmcnt(0)
	s_setprio 3
	v_mfma_f32_32x32x64_f8f6f4 v[48:63], v[0:5], v[96:101], 0 cbsz:2 blgp:2
	ds_read_b128 v[24:27], v124 offset:6144
	v_mfma_f32_32x32x64_f8f6f4 v[48:63], v[6:11], v[102:107], v[48:63] cbsz:2 blgp:2
	ds_read_b128 v[28:31], v124 offset:7168
	ds_read_b128 v[32:35], v124 offset:8192
	v_mfma_f32_32x32x64_f8f6f4 v[48:63], v[12:17], v[108:113], v[48:63] cbsz:2 blgp:2
	ds_read_b128 v[36:39], v124 offset:9216
	v_mfma_f32_32x32x64_f8f6f4 v[48:63], v[18:23], v[114:119], v[48:63] cbsz:2 blgp:2
	ds_read_b128 v[40:43], v124 offset:10240
	ds_read_b128 v[44:47], v124 offset:11264
	s_waitcnt vmcnt(3) lgkmcnt(0)
	s_barrier
	s_add_u32 s24, s10, 0xf000
	s_addc_u32 s25, s11, 0
	s_mov_b32 m0, s13
	s_nop 0
	global_load_lds_dwordx4 v124, s[24:25]
	v_mfma_f32_32x32x64_f8f6f4 v[64:79], v[24:29], v[96:101], 0 cbsz:2 blgp:2
	ds_read_b128 v[0:3], v124 offset:12288
	ds_read_b128 v[4:7], v124 offset:13312
	ds_read_b128 v[8:11], v124 offset:14336
	ds_read_b128 v[24:27], v124 offset:18432
	v_mfma_f32_32x32x64_f8f6f4 v[64:79], v[30:35], v[102:107], v[64:79] cbsz:2 blgp:2
	ds_read_b128 v[12:15], v124 offset:15360
	ds_read_b128 v[16:19], v124 offset:16384
	ds_read_b128 v[20:23], v124 offset:17408
	ds_read_b128 v[28:31], v124 offset:19456
	ds_read_b128 v[32:35], v124 offset:20480
	v_exp_f32_e32 v48, v48
	v_exp_f32_e32 v49, v49
	v_exp_f32_e32 v50, v50
	v_exp_f32_e32 v51, v51
	v_mfma_f32_32x32x64_f8f6f4 v[64:79], v[36:41], v[108:113], v[64:79] cbsz:2 blgp:2
	ds_read_b128 v[36:39], v124 offset:21504
	v_exp_f32_e32 v52, v52
	v_exp_f32_e32 v53, v53
	v_exp_f32_e32 v54, v54
	v_exp_f32_e32 v55, v55
	v_pk_add_f32 v[120:121], v[120:121], v[48:49]
	v_pk_add_f32 v[122:123], v[122:123], v[50:51]
	v_mfma_f32_32x32x64_f8f6f4 v[64:79], v[42:47], v[114:119], v[64:79] cbsz:2 blgp:2
	ds_read_b128 v[40:43], v124 offset:22528
	ds_read_b128 v[44:47], v124 offset:23552
	v_exp_f32_e32 v56, v56
	v_exp_f32_e32 v57, v57
	v_exp_f32_e32 v58, v58
	v_exp_f32_e32 v59, v59
	v_pk_add_f32 v[120:121], v[120:121], v[52:53]
	v_pk_add_f32 v[122:123], v[122:123], v[54:55]
	s_waitcnt vmcnt(3) lgkmcnt(5)
	s_barrier
	v_mfma_f32_32x32x64_f8f6f4 v[80:95], v[0:5], v[96:101], 0 cbsz:2 blgp:2
	ds_read_b128 v[0:3], v124 offset:24576
	v_exp_f32_e32 v60, v60
	v_exp_f32_e32 v61, v61
	v_exp_f32_e32 v62, v62
	v_exp_f32_e32 v63, v63
	v_pk_add_f32 v[120:121], v[120:121], v[56:57]
	v_pk_add_f32 v[122:123], v[122:123], v[58:59]
	v_mfma_f32_32x32x64_f8f6f4 v[80:95], v[6:11], v[102:107], v[80:95] cbsz:2 blgp:2
	ds_read_b128 v[4:7], v124 offset:25600
	ds_read_b128 v[8:11], v124 offset:26624
	v_exp_f32_e32 v64, v64
	v_exp_f32_e32 v65, v65
	v_exp_f32_e32 v66, v66
	v_exp_f32_e32 v67, v67
	v_pk_add_f32 v[120:121], v[120:121], v[60:61]
	v_pk_add_f32 v[122:123], v[122:123], v[62:63]
	v_mfma_f32_32x32x64_f8f6f4 v[80:95], v[12:17], v[108:113], v[80:95] cbsz:2 blgp:2
	ds_read_b128 v[12:15], v124 offset:27648
	v_exp_f32_e32 v68, v68
	v_exp_f32_e32 v69, v69
	v_exp_f32_e32 v70, v70
	v_exp_f32_e32 v71, v71
	v_pk_add_f32 v[120:121], v[120:121], v[64:65]
	v_pk_add_f32 v[122:123], v[122:123], v[66:67]
	v_mfma_f32_32x32x64_f8f6f4 v[80:95], v[18:23], v[114:119], v[80:95] cbsz:2 blgp:2
	ds_read_b128 v[16:19], v124 offset:28672
	ds_read_b128 v[20:23], v124 offset:29696
	v_exp_f32_e32 v72, v72
	v_exp_f32_e32 v73, v73
	v_exp_f32_e32 v74, v74
	v_exp_f32_e32 v75, v75
	v_pk_add_f32 v[120:121], v[120:121], v[68:69]
	v_pk_add_f32 v[122:123], v[122:123], v[70:71]
	s_waitcnt lgkmcnt(6)
	v_mfma_f32_32x32x64_f8f6f4 v[48:63], v[24:29], v[96:101], 0 cbsz:2 blgp:2
	ds_read_b128 v[24:27], v124 offset:30720
	v_exp_f32_e32 v76, v76
	v_exp_f32_e32 v77, v77
	v_exp_f32_e32 v78, v78
	v_exp_f32_e32 v79, v79
	v_pk_add_f32 v[120:121], v[120:121], v[72:73]
	v_pk_add_f32 v[122:123], v[122:123], v[74:75]
	v_mfma_f32_32x32x64_f8f6f4 v[48:63], v[30:35], v[102:107], v[48:63] cbsz:2 blgp:2
	ds_read_b128 v[28:31], v124 offset:31744
	ds_read_b128 v[32:35], v124 offset:32768
	v_exp_f32_e32 v80, v80
	v_exp_f32_e32 v81, v81
	v_exp_f32_e32 v82, v82
	v_exp_f32_e32 v83, v83
	v_pk_add_f32 v[120:121], v[120:121], v[76:77]
	v_pk_add_f32 v[122:123], v[122:123], v[78:79]
	v_mfma_f32_32x32x64_f8f6f4 v[48:63], v[36:41], v[108:113], v[48:63] cbsz:2 blgp:2
	ds_read_b128 v[36:39], v124 offset:33792
	v_exp_f32_e32 v84, v84
	v_exp_f32_e32 v85, v85
	v_exp_f32_e32 v86, v86
	v_exp_f32_e32 v87, v87
	v_pk_add_f32 v[120:121], v[120:121], v[80:81]
	v_pk_add_f32 v[122:123], v[122:123], v[82:83]
	v_mfma_f32_32x32x64_f8f6f4 v[48:63], v[42:47], v[114:119], v[48:63] cbsz:2 blgp:2
	ds_read_b128 v[40:43], v124 offset:34816
	ds_read_b128 v[44:47], v124 offset:35840
	v_exp_f32_e32 v88, v88
	v_exp_f32_e32 v89, v89
	v_exp_f32_e32 v90, v90
	v_exp_f32_e32 v91, v91
	v_pk_add_f32 v[120:121], v[120:121], v[84:85]
	v_pk_add_f32 v[122:123], v[122:123], v[86:87]
	s_setprio 2
	s_waitcnt vmcnt(2) lgkmcnt(6)
	s_barrier
	v_mfma_f32_32x32x64_f8f6f4 v[64:79], v[0:5], v[96:101], 0 cbsz:2 blgp:2
	ds_read_b128 v[0:3], v124 offset:36864
	v_exp_f32_e32 v92, v92
	v_exp_f32_e32 v93, v93
	v_exp_f32_e32 v94, v94
	v_exp_f32_e32 v95, v95
	v_pk_add_f32 v[120:121], v[120:121], v[88:89]
	v_pk_add_f32 v[122:123], v[122:123], v[90:91]
	v_mfma_f32_32x32x64_f8f6f4 v[64:79], v[6:11], v[102:107], v[64:79] cbsz:2 blgp:2
	ds_read_b128 v[4:7], v124 offset:37888
	ds_read_b128 v[8:11], v124 offset:38912
	v_exp_f32_e32 v48, v48
	v_exp_f32_e32 v49, v49
	v_exp_f32_e32 v50, v50
	v_exp_f32_e32 v51, v51
	v_pk_add_f32 v[120:121], v[120:121], v[92:93]
	v_pk_add_f32 v[122:123], v[122:123], v[94:95]
	v_mfma_f32_32x32x64_f8f6f4 v[64:79], v[12:17], v[108:113], v[64:79] cbsz:2 blgp:2
	ds_read_b128 v[12:15], v124 offset:39936
	v_exp_f32_e32 v52, v52
	v_exp_f32_e32 v53, v53
	v_exp_f32_e32 v54, v54
	v_exp_f32_e32 v55, v55
	v_pk_add_f32 v[120:121], v[120:121], v[48:49]
	v_pk_add_f32 v[122:123], v[122:123], v[50:51]
	v_mfma_f32_32x32x64_f8f6f4 v[64:79], v[18:23], v[114:119], v[64:79] cbsz:2 blgp:2
	ds_read_b128 v[16:19], v124 offset:40960
	ds_read_b128 v[20:23], v124 offset:41984
	v_exp_f32_e32 v56, v56
	v_exp_f32_e32 v57, v57
	v_exp_f32_e32 v58, v58
	v_exp_f32_e32 v59, v59
	v_pk_add_f32 v[120:121], v[120:121], v[52:53]
	v_pk_add_f32 v[122:123], v[122:123], v[54:55]
	s_waitcnt lgkmcnt(6)
	v_mfma_f32_32x32x64_f8f6f4 v[80:95], v[24:29], v[96:101], 0 cbsz:2 blgp:2
	ds_read_b128 v[24:27], v124 offset:43008
	v_exp_f32_e32 v60, v60
	v_exp_f32_e32 v61, v61
	v_exp_f32_e32 v62, v62
	v_exp_f32_e32 v63, v63
	v_pk_add_f32 v[120:121], v[120:121], v[56:57]
	v_pk_add_f32 v[122:123], v[122:123], v[58:59]
	v_mfma_f32_32x32x64_f8f6f4 v[80:95], v[30:35], v[102:107], v[80:95] cbsz:2 blgp:2
	ds_read_b128 v[28:31], v124 offset:44032
	ds_read_b128 v[32:35], v124 offset:45056
	v_exp_f32_e32 v64, v64
	v_exp_f32_e32 v65, v65
	v_exp_f32_e32 v66, v66
	v_exp_f32_e32 v67, v67
	v_pk_add_f32 v[120:121], v[120:121], v[60:61]
	v_pk_add_f32 v[122:123], v[122:123], v[62:63]
	v_mfma_f32_32x32x64_f8f6f4 v[80:95], v[36:41], v[108:113], v[80:95] cbsz:2 blgp:2
	ds_read_b128 v[36:39], v124 offset:46080
	v_exp_f32_e32 v68, v68
	v_exp_f32_e32 v69, v69
	v_exp_f32_e32 v70, v70
	v_exp_f32_e32 v71, v71
	v_pk_add_f32 v[120:121], v[120:121], v[64:65]
	v_pk_add_f32 v[122:123], v[122:123], v[66:67]
	v_mfma_f32_32x32x64_f8f6f4 v[80:95], v[42:47], v[114:119], v[80:95] cbsz:2 blgp:2
	ds_read_b128 v[40:43], v124 offset:47104
	ds_read_b128 v[44:47], v124 offset:48128
	v_exp_f32_e32 v72, v72
	v_exp_f32_e32 v73, v73
	v_exp_f32_e32 v74, v74
	v_exp_f32_e32 v75, v75
	v_pk_add_f32 v[120:121], v[120:121], v[68:69]
	v_pk_add_f32 v[122:123], v[122:123], v[70:71]
	s_waitcnt vmcnt(1) lgkmcnt(6)
	s_barrier
	v_mfma_f32_32x32x64_f8f6f4 v[48:63], v[0:5], v[96:101], 0 cbsz:2 blgp:2
	ds_read_b128 v[0:3], v124 offset:49152
	v_exp_f32_e32 v76, v76
	v_exp_f32_e32 v77, v77
	v_exp_f32_e32 v78, v78
	v_exp_f32_e32 v79, v79
	v_pk_add_f32 v[120:121], v[120:121], v[72:73]
	v_pk_add_f32 v[122:123], v[122:123], v[74:75]
	v_mfma_f32_32x32x64_f8f6f4 v[48:63], v[6:11], v[102:107], v[48:63] cbsz:2 blgp:2
	ds_read_b128 v[4:7], v124 offset:50176
	ds_read_b128 v[8:11], v124 offset:51200
	v_exp_f32_e32 v80, v80
	v_exp_f32_e32 v81, v81
	v_exp_f32_e32 v82, v82
	v_exp_f32_e32 v83, v83
	v_pk_add_f32 v[120:121], v[120:121], v[76:77]
	v_pk_add_f32 v[122:123], v[122:123], v[78:79]
	v_mfma_f32_32x32x64_f8f6f4 v[48:63], v[12:17], v[108:113], v[48:63] cbsz:2 blgp:2
	ds_read_b128 v[12:15], v124 offset:52224
	v_exp_f32_e32 v84, v84
	v_exp_f32_e32 v85, v85
	v_exp_f32_e32 v86, v86
	v_exp_f32_e32 v87, v87
	v_pk_add_f32 v[120:121], v[120:121], v[80:81]
	v_pk_add_f32 v[122:123], v[122:123], v[82:83]
	v_mfma_f32_32x32x64_f8f6f4 v[48:63], v[18:23], v[114:119], v[48:63] cbsz:2 blgp:2
	ds_read_b128 v[16:19], v124 offset:53248
	ds_read_b128 v[20:23], v124 offset:54272
	v_exp_f32_e32 v88, v88
	v_exp_f32_e32 v89, v89
	v_exp_f32_e32 v90, v90
	v_exp_f32_e32 v91, v91
	v_pk_add_f32 v[120:121], v[120:121], v[84:85]
	v_pk_add_f32 v[122:123], v[122:123], v[86:87]
	s_waitcnt lgkmcnt(6)
	v_mfma_f32_32x32x64_f8f6f4 v[64:79], v[24:29], v[96:101], 0 cbsz:2 blgp:2
	ds_read_b128 v[24:27], v124 offset:55296
	v_exp_f32_e32 v92, v92
	v_exp_f32_e32 v93, v93
	v_exp_f32_e32 v94, v94
	v_exp_f32_e32 v95, v95
	v_pk_add_f32 v[120:121], v[120:121], v[88:89]
	v_pk_add_f32 v[122:123], v[122:123], v[90:91]
	v_mfma_f32_32x32x64_f8f6f4 v[64:79], v[30:35], v[102:107], v[64:79] cbsz:2 blgp:2
	ds_read_b128 v[28:31], v124 offset:56320
	ds_read_b128 v[32:35], v124 offset:57344
	v_exp_f32_e32 v48, v48
	v_exp_f32_e32 v49, v49
	v_exp_f32_e32 v50, v50
	v_exp_f32_e32 v51, v51
	v_pk_add_f32 v[120:121], v[120:121], v[92:93]
	v_pk_add_f32 v[122:123], v[122:123], v[94:95]
	v_mfma_f32_32x32x64_f8f6f4 v[64:79], v[36:41], v[108:113], v[64:79] cbsz:2 blgp:2
	ds_read_b128 v[36:39], v124 offset:58368
	v_exp_f32_e32 v52, v52
	v_exp_f32_e32 v53, v53
	v_exp_f32_e32 v54, v54
	v_exp_f32_e32 v55, v55
	v_pk_add_f32 v[120:121], v[120:121], v[48:49]
	v_pk_add_f32 v[122:123], v[122:123], v[50:51]
	v_mfma_f32_32x32x64_f8f6f4 v[64:79], v[42:47], v[114:119], v[64:79] cbsz:2 blgp:2
	ds_read_b128 v[40:43], v124 offset:59392
	ds_read_b128 v[44:47], v124 offset:60416
	v_exp_f32_e32 v56, v56
	v_exp_f32_e32 v57, v57
	v_exp_f32_e32 v58, v58
	v_exp_f32_e32 v59, v59
	v_pk_add_f32 v[120:121], v[120:121], v[52:53]
	v_pk_add_f32 v[122:123], v[122:123], v[54:55]
	s_setprio 1
	s_waitcnt vmcnt(0) lgkmcnt(6)
	s_barrier
	v_mfma_f32_32x32x64_f8f6f4 v[80:95], v[0:5], v[96:101], 0 cbsz:2 blgp:2
	ds_read_b128 v[0:3], v124
	v_exp_f32_e32 v60, v60
	v_exp_f32_e32 v61, v61
	v_exp_f32_e32 v62, v62
	v_exp_f32_e32 v63, v63
	v_pk_add_f32 v[120:121], v[120:121], v[56:57]
	v_pk_add_f32 v[122:123], v[122:123], v[58:59]
	v_mfma_f32_32x32x64_f8f6f4 v[80:95], v[6:11], v[102:107], v[80:95] cbsz:2 blgp:2
	ds_read_b128 v[4:7], v124 offset:1024
	ds_read_b128 v[8:11], v124 offset:2048
	v_exp_f32_e32 v64, v64
	v_exp_f32_e32 v65, v65
	v_exp_f32_e32 v66, v66
	v_exp_f32_e32 v67, v67
	v_pk_add_f32 v[120:121], v[120:121], v[60:61]
	v_pk_add_f32 v[122:123], v[122:123], v[62:63]
	v_mfma_f32_32x32x64_f8f6f4 v[80:95], v[12:17], v[108:113], v[80:95] cbsz:2 blgp:2
	ds_read_b128 v[12:15], v124 offset:3072
	v_exp_f32_e32 v68, v68
	v_exp_f32_e32 v69, v69
	v_exp_f32_e32 v70, v70
	v_exp_f32_e32 v71, v71
	v_pk_add_f32 v[120:121], v[120:121], v[64:65]
	v_pk_add_f32 v[122:123], v[122:123], v[66:67]
	v_mfma_f32_32x32x64_f8f6f4 v[80:95], v[18:23], v[114:119], v[80:95] cbsz:2 blgp:2
	ds_read_b128 v[16:19], v124 offset:4096
	ds_read_b128 v[20:23], v124 offset:5120
	v_exp_f32_e32 v72, v72
	v_exp_f32_e32 v73, v73
	v_exp_f32_e32 v74, v74
	v_exp_f32_e32 v75, v75
	v_pk_add_f32 v[120:121], v[120:121], v[68:69]
	v_pk_add_f32 v[122:123], v[122:123], v[70:71]
	s_waitcnt lgkmcnt(6)
	v_mfma_f32_32x32x64_f8f6f4 v[48:63], v[24:29], v[96:101], 0 cbsz:2 blgp:2
	ds_read_b128 v[24:27], v124 offset:6144
	v_exp_f32_e32 v76, v76
	v_exp_f32_e32 v77, v77
	v_exp_f32_e32 v78, v78
	v_exp_f32_e32 v79, v79
	v_pk_add_f32 v[120:121], v[120:121], v[72:73]
	v_pk_add_f32 v[122:123], v[122:123], v[74:75]
	v_mfma_f32_32x32x64_f8f6f4 v[48:63], v[30:35], v[102:107], v[48:63] cbsz:2 blgp:2
	ds_read_b128 v[28:31], v124 offset:7168
	ds_read_b128 v[32:35], v124 offset:8192
	v_exp_f32_e32 v80, v80
	v_exp_f32_e32 v81, v81
	v_exp_f32_e32 v82, v82
	v_exp_f32_e32 v83, v83
	v_pk_add_f32 v[120:121], v[120:121], v[76:77]
	v_pk_add_f32 v[122:123], v[122:123], v[78:79]
	s_cmp_lg_u32 s8, 10
	s_cbranch_scc1 .Lmk_nosplit_b
	v_add_f32_e32 v127, v120, v121
	v_add_f32_e32 v126, v122, v123
	v_mov_b32_e32 v120, 0
	v_mov_b32_e32 v121, 0
	v_mov_b32_e32 v122, 0
	v_mov_b32_e32 v123, 0
	v_add_f32_e32 v127, v127, v126
.Lmk_nosplit_b:
	v_mfma_f32_32x32x64_f8f6f4 v[48:63], v[36:41], v[108:113], v[48:63] cbsz:2 blgp:2
	ds_read_b128 v[36:39], v124 offset:9216
	v_exp_f32_e32 v84, v84
	v_exp_f32_e32 v85, v85
	v_exp_f32_e32 v86, v86
	v_exp_f32_e32 v87, v87
	v_pk_add_f32 v[120:121], v[120:121], v[80:81]
	v_pk_add_f32 v[122:123], v[122:123], v[82:83]
	v_mfma_f32_32x32x64_f8f6f4 v[48:63], v[42:47], v[114:119], v[48:63] cbsz:2 blgp:2
	ds_read_b128 v[40:43], v124 offset:10240
	ds_read_b128 v[44:47], v124 offset:11264
	v_exp_f32_e32 v88, v88
	v_exp_f32_e32 v89, v89
	v_exp_f32_e32 v90, v90
	v_exp_f32_e32 v91, v91
	v_pk_add_f32 v[120:121], v[120:121], v[84:85]
	v_pk_add_f32 v[122:123], v[122:123], v[86:87]
	s_setprio 0
	s_waitcnt lgkmcnt(6)
	v_mfma_f32_32x32x64_f8f6f4 v[64:79], v[0:5], v[96:101], 0 cbsz:2 blgp:2
	v_exp_f32_e32 v92, v92
	v_exp_f32_e32 v93, v93
	v_exp_f32_e32 v94, v94
	v_exp_f32_e32 v95, v95
	v_pk_add_f32 v[120:121], v[120:121], v[88:89]
	v_pk_add_f32 v[122:123], v[122:123], v[90:91]
	v_mfma_f32_32x32x64_f8f6f4 v[64:79], v[6:11], v[102:107], v[64:79] cbsz:2 blgp:2
	v_exp_f32_e32 v48, v48
	v_exp_f32_e32 v49, v49
	v_exp_f32_e32 v50, v50
	v_exp_f32_e32 v51, v51
	v_pk_add_f32 v[120:121], v[120:121], v[92:93]
	v_pk_add_f32 v[122:123], v[122:123], v[94:95]
	v_mfma_f32_32x32x64_f8f6f4 v[64:79], v[12:17], v[108:113], v[64:79] cbsz:2 blgp:2
	v_exp_f32_e32 v52, v52
	v_exp_f32_e32 v53, v53
	v_exp_f32_e32 v54, v54
	v_exp_f32_e32 v55, v55
	v_pk_add_f32 v[120:121], v[120:121], v[48:49]
	v_pk_add_f32 v[122:123], v[122:123], v[50:51]
	v_mfma_f32_32x32x64_f8f6f4 v[64:79], v[18:23], v[114:119], v[64:79] cbsz:2 blgp:2
	v_exp_f32_e32 v56, v56
	v_exp_f32_e32 v57, v57
	v_exp_f32_e32 v58, v58
	v_exp_f32_e32 v59, v59
	v_pk_add_f32 v[120:121], v[120:121], v[52:53]
	v_pk_add_f32 v[122:123], v[122:123], v[54:55]
	s_waitcnt lgkmcnt(0)
	v_mfma_f32_32x32x64_f8f6f4 v[80:95], v[24:29], v[96:101], 0 cbsz:2 blgp:2
	v_exp_f32_e32 v60, v60
	v_exp_f32_e32 v61, v61
	v_exp_f32_e32 v62, v62
	v_exp_f32_e32 v63, v63
	v_pk_add_f32 v[120:121], v[120:121], v[56:57]
	v_pk_add_f32 v[122:123], v[122:123], v[58:59]
	v_mfma_f32_32x32x64_f8f6f4 v[80:95], v[30:35], v[102:107], v[80:95] cbsz:2 blgp:2
	v_exp_f32_e32 v64, v64
	v_exp_f32_e32 v65, v65
	v_exp_f32_e32 v66, v66
	v_exp_f32_e32 v67, v67
	v_pk_add_f32 v[120:121], v[120:121], v[60:61]
	v_pk_add_f32 v[122:123], v[122:123], v[62:63]
	v_mfma_f32_32x32x64_f8f6f4 v[80:95], v[36:41], v[108:113], v[80:95] cbsz:2 blgp:2
	v_exp_f32_e32 v68, v68
	v_exp_f32_e32 v69, v69
	v_exp_f32_e32 v70, v70
	v_exp_f32_e32 v71, v71
	v_pk_add_f32 v[120:121], v[120:121], v[64:65]
	v_pk_add_f32 v[122:123], v[122:123], v[66:67]
	v_mfma_f32_32x32x64_f8f6f4 v[80:95], v[42:47], v[114:119], v[80:95] cbsz:2 blgp:2
	v_exp_f32_e32 v72, v72
	v_exp_f32_e32 v73, v73
	v_exp_f32_e32 v74, v74
	v_exp_f32_e32 v75, v75
	v_pk_add_f32 v[120:121], v[120:121], v[68:69]
	v_pk_add_f32 v[122:123], v[122:123], v[70:71]
	v_exp_f32_e32 v76, v76
	v_exp_f32_e32 v77, v77
	v_exp_f32_e32 v78, v78
	v_exp_f32_e32 v79, v79
	v_pk_add_f32 v[120:121], v[120:121], v[72:73]
	v_pk_add_f32 v[122:123], v[122:123], v[74:75]
	s_nop 1
	v_exp_f32_e32 v80, v80
	v_exp_f32_e32 v81, v81
	v_exp_f32_e32 v82, v82
	v_exp_f32_e32 v83, v83
	v_pk_add_f32 v[120:121], v[120:121], v[76:77]
	v_pk_add_f32 v[122:123], v[122:123], v[78:79]
	v_exp_f32_e32 v84, v84
	v_exp_f32_e32 v85, v85
	v_exp_f32_e32 v86, v86
	v_exp_f32_e32 v87, v87
	v_pk_add_f32 v[120:121], v[120:121], v[80:81]
	v_pk_add_f32 v[122:123], v[122:123], v[82:83]
	v_exp_f32_e32 v88, v88
	v_exp_f32_e32 v89, v89
	v_exp_f32_e32 v90, v90
	v_exp_f32_e32 v91, v91
	v_pk_add_f32 v[120:121], v[120:121], v[84:85]
	v_pk_add_f32 v[122:123], v[122:123], v[86:87]
	v_exp_f32_e32 v92, v92
	v_exp_f32_e32 v93, v93
	v_exp_f32_e32 v94, v94
	v_exp_f32_e32 v95, v95
	v_pk_add_f32 v[120:121], v[120:121], v[88:89]
	v_pk_add_f32 v[122:123], v[122:123], v[90:91]
	v_pk_add_f32 v[120:121], v[120:121], v[92:93]
	v_pk_add_f32 v[122:123], v[122:123], v[94:95]
	v_add_f32_e32 v120, v120, v121
	v_add_f32_e32 v122, v122, v123
	v_lshrrev_b32_e32 v126, 2, v124
	v_add_f32_e32 v120, v120, v122
	v_xor_b32_e32 v125, 0x80, v126
	s_mov_b64 s[4:5], s[30:31]
	s_mov_b64 s[6:7], s[32:33]
	ds_bpermute_b32 v122, v125, v120
	ds_bpermute_b32 v123, v125, v127
	s_lshl_b32 s14, s14, 7
	v_add_u32_e32 v126, s14, v126
	v_cmp_gt_u32_e32 vcc, 0x200, v124
	s_and_saveexec_b64 s[16:17], vcc
	s_cbranch_execz .Lmk_end_b
	s_waitcnt lgkmcnt(0)
	v_add_f32_e32 v120, v120, v122
	v_add_f32_e32 v127, v127, v123
	s_cmp_lt_u32 s8, 10
	s_cbranch_scc1 .Lmk_pos_only_b
	s_cmp_eq_u32 s8, 10
	s_cbranch_scc0 .Lmk_neg_only_b
	global_atomic_add_f32 v126, v127, s[4:5]
